# LN1 row loop: the 8 loop-invariant gamma/beta loads per row are loaded once before the loop (register moves in the loop); counted waits recomputed
# speedup vs baseline: 1.0101x; 1.0075x over previous
; #define GAS __attribute__((address_space(1)))
; __device__ __forceinline__ void unpack8(const u32x4 q, float* o) { o[0] = bflo(q.x); o[1] = bfhi(q.x); o[2] = bflo(q.y); o[3] = bfhi(q.y); o[4] = bflo(q.z); o[5] = bfhi(q.z); o[6] = bflo(q.w); o[7] = bfhi(q.w); }
; __device__ __forceinline__ void ph_ln1(Frame& F, int l, int ntok) {
;     const int gw = F.wg * NWAVES + F.wave, NGW = F.G * NWAVES;
;     const int cA = 256 * (F.lane >> 4) + 32 * ((F.lane >> 2) & 3) + 8 * (F.lane & 3);
;     ...
;     const float* lg = F.in[I_LN1G] + l * DM; const float* lb = F.in[I_LN1B] + l * DM;
;     for (int row = gw; row < ntok; row += NGW) {
;         bf16_t* xr = (bf16_t*)(F.ws + WS_XR) + (size_t)row * DM;
;         const unsigned char* yr = (const unsigned char*)(F.ws + WS_Y) + (size_t)row * DM + 16 * F.lane;
;         const float* md = mod_ptr(F, l, row);
;         const u32x4 xa = __builtin_nontemporal_load((const GAS u32x4*)(xr + cA)), xb = __builtin_nontemporal_load((const GAS u32x4*)(xr + cA + 128)), ya = __builtin_nontemporal_load((const GAS u32x4*)yr);
;         float x[16], y[16], v[16]; unpack8(xa, x); unpack8(xb, x + 8);
;         { const unsigned a[4] = {ya.x, ya.y, ya.z, ya.w};
; #pragma unroll
;           for (int e = 0; e < 4; ++e) { const f32x2 lo = __builtin_amdgcn_cvt_pk_f32_fp8((int)a[e], false), hi = __builtin_amdgcn_cvt_pk_f32_fp8((int)a[e], true); y[4 * e] = lo.x; y[4 * e + 1] = lo.y; y[4 * e + 2] = hi.x; y[4 * e + 3] = hi.y; } }
;         float s = 0.f;
; #pragma unroll
;         for (int j = 0; j < 4; ++j) { const f32x4 g1 = *(const GAS f32x4*)(md + 2048 + LN1_COL(j));
; #pragma unroll
;             for (int e = 0; e < 4; ++e) { v[4 * j + e] = x[4 * j + e] * DN_ALPHA + g1[e] * y[4 * j + e]; s += v[4 * j + e]; } }
;         const float mean = wave_sum(s, F.lane) * (1.f / DM); float s2 = 0.f;
; #pragma unroll
;         for (int e = 0; e < 16; ++e) { v[e] -= mean; s2 += v[e] * v[e]; }
;         const float rstd = 1.f / sqrtf(wave_sum(s2, F.lane) * (1.f / DM) + LN_EPS);
;         unsigned wx[8]; int w8[4];
; #pragma unroll
;         for (int j = 0; j < 4; ++j) { const f32x4 g = *(const GAS f32x4*)(lg + LN1_COL(j)), bb = *(const GAS f32x4*)(lb + LN1_COL(j)), sh = *(const GAS f32x4*)(md + 3072 + LN1_COL(j)), sc = *(const GAS f32x4*)(md + 4096 + LN1_COL(j));
.LBB0_772:
	s_andn2_b64 vcc, exec, s[2:3]
	s_cbranch_vccnz .LBB0_826
	v_readlane_b32 s36, v252, 8
	v_readlane_b32 s37, v252, 9
	s_mov_b32 s0, s97
	v_readlane_b32 s38, v252, 10
	v_readlane_b32 s39, v252, 11
	s_mov_b64 s[2:3], s[36:37]
	v_mbcnt_lo_u32_b32 v0, -1, 0
	v_mbcnt_hi_u32_b32 v0, -1, v0
	v_readlane_b32 s8, v255, 14
	v_readlane_b32 s2, v254, 28
	s_add_i32 s40, s0, s2
	v_readlane_b32 s9, v255, 15
	v_readlane_b32 s10, v255, 3
	v_readlane_b32 s18, v255, 5
	s_cmp_ge_i32 s40, s80
	v_readlane_b32 s11, v255, 4
	v_readlane_b32 s19, v255, 6
	s_mov_b32 s9, 0xf800000
	s_mov_b32 s20, 0x3fd744fd
	s_cbranch_scc1 .LBB0_776
	s_lshl_b32 s22, s30, 10
	v_readlane_b32 s44, v252, 16
	s_lshl_b64 s[2:3], s[22:23], 2
	v_readlane_b32 s46, v252, 18
	v_readlane_b32 s47, v252, 19
	s_add_u32 s4, s46, s2
	s_addc_u32 s5, s47, s3
	v_lshlrev_b32_e32 v1, 3, v0
	v_readlane_b32 s45, v252, 17
	s_add_u32 s2, s44, s2
	v_lshlrev_b32_e32 v2, 4, v0
	v_and_b32_e32 v1, 0x78, v1
	s_movk_i32 s0, 0xff00
	s_addc_u32 s3, s45, s3
	s_waitcnt vmcnt(0)
	v_and_or_b32 v4, v2, s0, v1
	v_ashrrev_i32_e32 v5, 31, v4
	s_add_u32 s22, s38, 0x100000
	v_lshlrev_b64 v[54:55], 2, v[4:5]
	s_addc_u32 s42, s39, 0
	s_ashr_i32 s41, s40, 31
	v_lshl_add_u64 v[56:57], s[2:3], 0, v[54:55]
	v_lshl_add_u64 v[58:59], s[4:5], 0, v[54:55]
	s_lshl_b64 s[2:3], s[40:41], 10
	s_lshl_b64 s[4:5], s[40:41], 11
	v_or_b32_e32 v6, 0x80, v4
	v_lshl_add_u64 v[60:61], s[2:3], 0, v[4:5]
	s_add_u32 s2, s2, 0x52900000
	v_ashrrev_i32_e32 v7, 31, v6
	v_ashrrev_i32_e32 v3, 31, v2
	v_lshlrev_b32_e32 v0, 2, v0
	s_addc_u32 s3, s3, 0
	v_xor_b32_e32 v76, 4, v0
	v_xor_b32_e32 v77, 8, v0
	v_xor_b32_e32 v78, 16, v0
	v_xor_b32_e32 v79, 32, v0
	v_xor_b32_e32 v80, 64, v0
	v_xor_b32_e32 v81, 0x80, v0
	v_lshl_add_u64 v[62:63], v[4:5], 1, s[4:5]
	v_lshl_add_u64 v[64:65], s[2:3], 0, v[2:3]
	v_lshlrev_b64 v[66:67], 2, v[6:7]
	v_readlane_b32 s48, v252, 20
	v_readlane_b32 s49, v252, 21
	v_readlane_b32 s50, v252, 22
	v_readlane_b32 s51, v252, 23
	v_readlane_b32 s52, v252, 24
	v_readlane_b32 s53, v252, 25
	v_readlane_b32 s54, v252, 26
	v_readlane_b32 s55, v252, 27
	v_readlane_b32 s56, v252, 28
	v_readlane_b32 s57, v252, 29
	v_readlane_b32 s58, v252, 30
	v_readlane_b32 s59, v252, 31
	s_brev_b32 s84, 38
	s_mov_b32 s85, 0
	v_lshl_add_u64 v[148:149], s[38:39], 0, v[62:63]
	v_lshl_add_u64 v[148:149], v[148:149], 0, s[84:85]
	v_lshl_add_u64 v[150:151], s[38:39], 0, v[64:65]
	global_load_dwordx4 v[128:131], v[148:149], off nt
	global_load_dwordx4 v[132:135], v[148:149], off offset:256 nt
	global_load_dwordx4 v[144:147], v[150:151], off nt
	global_load_dwordx4 v[156:159], v[56:57], off offset:16
	global_load_dwordx4 v[160:163], v[56:57], off
	global_load_dwordx4 v[164:167], v[58:59], off offset:16
	global_load_dwordx4 v[168:171], v[58:59], off
	global_load_dwordx4 v[172:175], v[56:57], off offset:528
	global_load_dwordx4 v[176:179], v[56:57], off offset:512
	global_load_dwordx4 v[180:183], v[58:59], off offset:528
	global_load_dwordx4 v[184:187], v[58:59], off offset:512
.LBB0_775:
	s_min_i32 s0, s40, 0x10000
	s_ashr_i32 s0, s0, 12
	s_ashr_i32 s2, s0, 31
	s_mul_i32 s3, s30, 17
	s_add_u32 s0, s0, s3
	s_addc_u32 s2, s2, 0
	s_mulk_i32 s2, 0x6000
	s_mul_hi_u32 s3, s0, 0x6000
	s_add_i32 s3, s3, s2
	v_lshl_add_u64 v[2:3], s[38:39], 0, v[62:63]
	s_brev_b32 s2, 38
	v_add_co_u32_e32 v68, vcc, s2, v2
	v_lshl_add_u64 v[0:1], s[38:39], 0, v[64:65]
	s_nop 0
	v_addc_co_u32_e32 v69, vcc, 0, v3, vcc
	s_nop 0
	s_mulk_i32 s0, 0x6000
	s_add_u32 s0, s22, s0
	s_addc_u32 s4, s42, s3
	s_add_u32 s2, s0, 0x2000
	s_addc_u32 s3, s4, 0
	s_add_u32 s36, s0, 0x3000
	s_addc_u32 s37, s4, 0
	v_lshl_add_u64 v[62:63], v[62:63], 0, s[18:19]
	v_lshl_add_u64 v[64:65], v[64:65], 0, s[10:11]
	s_waitcnt vmcnt(0)
	v_mov_b32_e32 v46, v128
	v_mov_b32_e32 v47, v129
	v_mov_b32_e32 v48, v130
	v_mov_b32_e32 v49, v131
	v_mov_b32_e32 v90, v132
	v_mov_b32_e32 v91, v133
	v_mov_b32_e32 v92, v134
	v_mov_b32_e32 v93, v135
	v_mov_b32_e32 v0, v144
	v_mov_b32_e32 v1, v145
	v_mov_b32_e32 v2, v146
	v_mov_b32_e32 v3, v147
	v_lshlrev_b32_e32 v122, 16, v93
	v_cvt_pk_f32_fp8_e32 v[24:25], v0
	v_cvt_pk_f32_fp8_sdwa v[70:71], v0 src0_sel:WORD_1
	v_cvt_pk_f32_fp8_e32 v[72:73], v1
	v_cvt_pk_f32_fp8_sdwa v[74:75], v1 src0_sel:WORD_1
	v_lshl_add_u64 v[0:1], s[2:3], 0, v[54:55]
	global_load_dwordx4 v[50:53], v[0:1], off
	global_load_dwordx4 v[94:97], v[0:1], off offset:16
	v_lshl_add_u64 v[0:1], s[2:3], 0, v[66:67]
	global_load_dwordx4 v[98:101], v[0:1], off
	global_load_dwordx4 v[102:105], v[0:1], off offset:16
	s_add_u32 s2, s0, 0x4000
	s_addc_u32 s3, s4, 0
	v_lshl_add_u64 v[0:1], s[36:37], 0, v[54:55]
	v_lshl_add_u64 v[4:5], s[2:3], 0, v[54:55]
	v_cvt_pk_f32_fp8_e32 v[114:115], v2
	v_cvt_pk_f32_fp8_sdwa v[116:117], v2 src0_sel:WORD_1
	v_cvt_pk_f32_fp8_e32 v[118:119], v3
	v_cvt_pk_f32_fp8_sdwa v[120:121], v3 src0_sel:WORD_1
	v_mov_b32_e32 v26, v156
	v_mov_b32_e32 v27, v157
	v_mov_b32_e32 v28, v158
	v_mov_b32_e32 v29, v159
	v_mov_b32_e32 v106, v160
	v_mov_b32_e32 v107, v161
	v_mov_b32_e32 v108, v162
	v_mov_b32_e32 v109, v163
	v_mov_b32_e32 v30, v164
	v_mov_b32_e32 v31, v165
	v_mov_b32_e32 v32, v166
	v_mov_b32_e32 v33, v167
	v_mov_b32_e32 v110, v168
	v_mov_b32_e32 v111, v169
	v_mov_b32_e32 v112, v170
	v_mov_b32_e32 v113, v171
	global_load_dwordx4 v[12:15], v[0:1], off offset:16
	global_load_dwordx4 v[42:45], v[0:1], off
	s_nop 0
	global_load_dwordx4 v[0:3], v[4:5], off offset:16
	s_nop 0
	global_load_dwordx4 v[4:7], v[4:5], off
	v_and_b32_e32 v123, 0xffff0000, v93
	v_lshl_add_u64 v[82:83], s[2:3], 0, v[66:67]
	s_waitcnt lgkmcnt(0)
; #define GAS __attribute__((address_space(1)))
; __device__ __forceinline__ void ph_ln1(Frame& F, int l, int ntok) {
;     ...
;         for (int j = 0; j < 4; ++j) { const f32x4 g1 = *(const GAS f32x4*)(md + 2048 + LN1_COL(j));
; #pragma unroll
;             for (int e = 0; e < 4; ++e) { v[4 * j + e] = x[4 * j + e] * DN_ALPHA + g1[e] * y[4 * j + e]; s += v[4 * j + e]; } }
;         const float mean = wave_sum(s, F.lane) * (1.f / DM); float s2 = 0.f;
; #pragma unroll
;         for (int e = 0; e < 16; ++e) { v[e] -= mean; s2 += v[e] * v[e]; }
;         const float rstd = 1.f / sqrtf(wave_sum(s2, F.lane) * (1.f / DM) + LN_EPS);
;         unsigned wx[8]; int w8[4];
; #pragma unroll
;         for (int j = 0; j < 4; ++j) { const f32x4 g = *(const GAS f32x4*)(lg + LN1_COL(j)), bb = *(const GAS f32x4*)(lb + LN1_COL(j)), sh = *(const GAS f32x4*)(md + 3072 + LN1_COL(j)), sc = *(const GAS f32x4*)(md + 4096 + LN1_COL(j));
	v_mov_b32_e32 v8, v172
	v_mov_b32_e32 v9, v173
	v_mov_b32_e32 v10, v174
	v_mov_b32_e32 v11, v175
	v_mov_b32_e32 v34, v176
	v_mov_b32_e32 v35, v177
	v_mov_b32_e32 v36, v178
	v_mov_b32_e32 v37, v179
	v_mov_b32_e32 v16, v180
	v_mov_b32_e32 v17, v181
	v_mov_b32_e32 v18, v182
	v_mov_b32_e32 v19, v183
	v_mov_b32_e32 v38, v184
	v_mov_b32_e32 v39, v185
	v_mov_b32_e32 v40, v186
	v_mov_b32_e32 v41, v187
	s_mov_b32 s0, 0x5be00000
	s_add_i32 s40, s40, s8
	s_cmp_lt_i32 s40, s80
	s_waitcnt vmcnt(7)
	v_pk_mul_f32 v[52:53], v[70:71], v[52:53]
	v_lshlrev_b32_e32 v70, 16, v46
	v_and_b32_e32 v71, 0xffff0000, v46
	v_pk_mul_f32 v[24:25], v[24:25], v[50:51]
	s_waitcnt vmcnt(4)
	v_pk_mul_f32 v[104:105], v[120:121], v[104:105]
	v_lshlrev_b32_e32 v120, 16, v92
	v_and_b32_e32 v121, 0xffff0000, v92
	v_pk_mul_f32 v[92:93], v[118:119], v[102:103]
	v_lshlrev_b32_e32 v102, 16, v91
	v_and_b32_e32 v103, 0xffff0000, v91
	v_pk_mul_f32 v[100:101], v[116:117], v[100:101]
	v_pk_fma_f32 v[24:25], v[70:71], s[20:21], v[24:25] op_sel_hi:[1,0,1]
	v_pk_fma_f32 v[100:101], v[102:103], s[20:21], v[100:101] op_sel_hi:[1,0,1]
	v_lshlrev_b32_e32 v102, 16, v90
	v_and_b32_e32 v103, 0xffff0000, v90
	v_pk_mul_f32 v[90:91], v[114:115], v[98:99]
	v_lshlrev_b32_e32 v98, 16, v49
	v_and_b32_e32 v99, 0xffff0000, v49
	v_pk_mul_f32 v[74:75], v[74:75], v[96:97]
	v_lshlrev_b32_e32 v96, 16, v48
	v_and_b32_e32 v97, 0xffff0000, v48
	v_pk_mul_f32 v[48:49], v[72:73], v[94:95]
	v_lshlrev_b32_e32 v72, 16, v47
	v_and_b32_e32 v73, 0xffff0000, v47
	v_add_f32_e32 v46, 0, v24
	v_pk_fma_f32 v[52:53], v[72:73], s[20:21], v[52:53] op_sel_hi:[1,0,1]
	v_add_f32_e32 v46, v25, v46
	v_add_f32_e32 v46, v52, v46
	v_pk_fma_f32 v[48:49], v[96:97], s[20:21], v[48:49] op_sel_hi:[1,0,1]
	v_add_f32_e32 v46, v53, v46
	v_add_f32_e32 v46, v48, v46
	v_pk_fma_f32 v[74:75], v[98:99], s[20:21], v[74:75] op_sel_hi:[1,0,1]
	v_add_f32_e32 v46, v49, v46
	v_add_f32_e32 v46, v74, v46
	v_pk_fma_f32 v[90:91], v[102:103], s[20:21], v[90:91] op_sel_hi:[1,0,1]
	v_add_f32_e32 v46, v75, v46
	v_add_f32_e32 v46, v90, v46
	v_add_f32_e32 v46, v91, v46
	v_add_f32_e32 v46, v100, v46
	v_pk_fma_f32 v[92:93], v[120:121], s[20:21], v[92:93] op_sel_hi:[1,0,1]
	v_add_f32_e32 v46, v101, v46
	v_add_f32_e32 v46, v92, v46
	v_pk_fma_f32 v[104:105], v[122:123], s[20:21], v[104:105] op_sel_hi:[1,0,1]
	v_add_f32_e32 v46, v93, v46
	v_add_f32_e32 v46, v104, v46
	v_add_f32_e32 v46, v105, v46
	ds_bpermute_b32 v47, v76, v46
	s_waitcnt vmcnt(0)
	v_add_f32_e32 v124, 1.0, v4
	v_add_f32_e32 v125, 1.0, v5
	v_lshl_add_u64 v[4:5], s[36:37], 0, v[66:67]
	v_add_f32_e32 v126, 1.0, v6
	s_waitcnt lgkmcnt(0)
	v_add_f32_e32 v46, v46, v47
	ds_bpermute_b32 v47, v77, v46
	v_add_f32_e32 v127, 1.0, v7
	v_add_f32_e32 v86, 1.0, v0
	v_add_f32_e32 v87, 1.0, v1
	v_add_f32_e32 v88, 1.0, v2
	s_waitcnt lgkmcnt(0)
	v_add_f32_e32 v46, v46, v47
	ds_bpermute_b32 v47, v78, v46
	v_add_f32_e32 v89, 1.0, v3
	global_load_dwordx4 v[0:3], v[4:5], off offset:16
	global_load_dwordx4 v[20:23], v[4:5], off
	s_nop 0
	global_load_dwordx4 v[4:7], v[82:83], off offset:16
	s_nop 0
	global_load_dwordx4 v[82:85], v[82:83], off
	s_cselect_b64 s[86:87], -1, 0
	v_lshl_add_u64 v[148:149], s[38:39], 0, v[62:63]
	v_lshl_add_u64 v[148:149], v[148:149], 0, s[84:85]
	v_lshl_add_u64 v[150:151], s[38:39], 0, v[64:65]
	v_cndmask_b32_e64 v148, v68, v148, s[86:87]
	v_cndmask_b32_e64 v149, v69, v149, s[86:87]
	v_cndmask_b32_e64 v150, v68, v150, s[86:87]
	v_cndmask_b32_e64 v151, v69, v151, s[86:87]
	global_load_dwordx4 v[128:131], v[148:149], off nt
	global_load_dwordx4 v[132:135], v[148:149], off offset:256 nt
	global_load_dwordx4 v[144:147], v[150:151], off nt
	s_waitcnt lgkmcnt(0)
	v_add_f32_e32 v46, v46, v47
	ds_bpermute_b32 v47, v79, v46
	s_waitcnt lgkmcnt(0)
	v_add_f32_e32 v46, v46, v47
	ds_bpermute_b32 v47, v80, v46
	s_waitcnt lgkmcnt(0)
	v_add_f32_e32 v46, v46, v47
	ds_bpermute_b32 v47, v81, v46
	s_waitcnt lgkmcnt(0)
	v_add_f32_e32 v46, v46, v47
	v_mul_f32_e32 v50, 0x3a800000, v46
	v_pk_add_f32 v[24:25], v[24:25], v[50:51] op_sel_hi:[1,0] neg_lo:[0,1] neg_hi:[0,1]
	v_pk_add_f32 v[96:97], v[52:53], v[50:51] op_sel_hi:[1,0] neg_lo:[0,1] neg_hi:[0,1]
	v_pk_mul_f32 v[94:95], v[24:25], v[24:25]
	v_pk_mul_f32 v[98:99], v[96:97], v[96:97]
	v_add_f32_e32 v94, v94, v95
	v_pk_add_f32 v[72:73], v[48:49], v[50:51] op_sel_hi:[1,0] neg_lo:[0,1] neg_hi:[0,1]
	v_add_f32_e32 v94, v98, v94
	v_pk_mul_f32 v[102:103], v[72:73], v[72:73]
	v_add_f32_e32 v94, v99, v94
	v_pk_add_f32 v[74:75], v[74:75], v[50:51] op_sel_hi:[1,0] neg_lo:[0,1] neg_hi:[0,1]
	v_add_f32_e32 v94, v102, v94
	v_pk_mul_f32 v[114:115], v[74:75], v[74:75]
	v_add_f32_e32 v94, v103, v94
	v_pk_add_f32 v[52:53], v[90:91], v[50:51] op_sel_hi:[1,0] neg_lo:[0,1] neg_hi:[0,1]
	v_add_f32_e32 v94, v114, v94
	v_pk_mul_f32 v[90:91], v[52:53], v[52:53]
	v_add_f32_e32 v94, v115, v94
	v_pk_add_f32 v[70:71], v[100:101], v[50:51] op_sel_hi:[1,0] neg_lo:[0,1] neg_hi:[0,1]
	v_add_f32_e32 v90, v90, v94
	v_pk_mul_f32 v[100:101], v[70:71], v[70:71]
	v_add_f32_e32 v90, v91, v90
	v_pk_add_f32 v[46:47], v[92:93], v[50:51] op_sel_hi:[1,0] neg_lo:[0,1] neg_hi:[0,1]
	v_add_f32_e32 v90, v100, v90
	v_pk_mul_f32 v[92:93], v[46:47], v[46:47]
	v_add_f32_e32 v90, v101, v90
	v_pk_add_f32 v[48:49], v[104:105], v[50:51] op_sel_hi:[1,0] neg_lo:[0,1] neg_hi:[0,1]
	v_add_f32_e32 v90, v92, v90
	v_pk_mul_f32 v[50:51], v[48:49], v[48:49]
	v_add_f32_e32 v90, v93, v90
	v_add_f32_e32 v50, v50, v90
	v_add_f32_e32 v50, v51, v50
	ds_bpermute_b32 v51, v76, v50
	s_waitcnt lgkmcnt(0)
; #define GAS __attribute__((address_space(1)))
; __device__ __forceinline__ unsigned pk2(float lo, float hi) { const f32x2 v = {lo, hi}; const bf16v2 b = __builtin_convertvector(v, bf16v2); return __builtin_bit_cast(unsigned, b); }
; __device__ __forceinline__ void ph_ln1(Frame& F, int l, int ntok) {
;     ...
;         const float mean = wave_sum(s, F.lane) * (1.f / DM); float s2 = 0.f;
; #pragma unroll
;         for (int e = 0; e < 16; ++e) { v[e] -= mean; s2 += v[e] * v[e]; }
;         const float rstd = 1.f / sqrtf(wave_sum(s2, F.lane) * (1.f / DM) + LN_EPS);
;         unsigned wx[8]; int w8[4];
; #pragma unroll
;         for (int j = 0; j < 4; ++j) { const f32x4 g = *(const GAS f32x4*)(lg + LN1_COL(j)), bb = *(const GAS f32x4*)(lb + LN1_COL(j)), sh = *(const GAS f32x4*)(md + 3072 + LN1_COL(j)), sc = *(const GAS f32x4*)(md + 4096 + LN1_COL(j));
;             float xn[4];
; #pragma unroll
;             for (int e = 0; e < 4; ++e) xn[e] = v[4 * j + e] * rstd * g[e] + bb[e];
;             wx[2 * j] = pk2(xn[0], xn[1]); wx[2 * j + 1] = pk2(xn[2], xn[3]);
;             const float h0 = xn[0] * (1.f + sc[0]) + sh[0], h1 = xn[1] * (1.f + sc[1]) + sh[1], h2 = xn[2] * (1.f + sc[2]) + sh[2], h3 = xn[3] * (1.f + sc[3]) + sh[3];
;             int v = 0; v = __builtin_amdgcn_cvt_pk_fp8_f32(h0, h1, v, false); v = __builtin_amdgcn_cvt_pk_fp8_f32(h2, h3, v, true); w8[j] = v; }
;         unsigned char* x8 = (unsigned char*)(F.ws + WS_XM8) + (size_t)row * DM;
;         __builtin_nontemporal_store((u32x2){(unsigned)w8[0], (unsigned)w8[1]}, (GAS u32x2*)(x8 + cA)); __builtin_nontemporal_store((u32x2){(unsigned)w8[2], (unsigned)w8[3]}, (GAS u32x2*)(x8 + cA + 128));
;         __builtin_nontemporal_store((u32x4){wx[0], wx[1], wx[2], wx[3]}, (GAS u32x4*)(xr + cA)); __builtin_nontemporal_store((u32x4){wx[4], wx[5], wx[6], wx[7]}, (GAS u32x4*)(xr + cA + 128));
	v_add_f32_e32 v50, v50, v51
	ds_bpermute_b32 v51, v77, v50
	s_waitcnt lgkmcnt(0)
	v_add_f32_e32 v50, v50, v51
	ds_bpermute_b32 v51, v78, v50
	s_waitcnt lgkmcnt(0)
	v_add_f32_e32 v50, v50, v51
	ds_bpermute_b32 v51, v79, v50
	s_waitcnt lgkmcnt(0)
	v_add_f32_e32 v50, v50, v51
	ds_bpermute_b32 v51, v80, v50
	s_waitcnt vmcnt(4)
	v_add_f32_e32 v4, 1.0, v4
	s_waitcnt vmcnt(3)
	v_add_f32_e32 v82, 1.0, v82
	v_add_f32_e32 v83, 1.0, v83
	s_waitcnt lgkmcnt(0)
	v_add_f32_e32 v50, v50, v51
	ds_bpermute_b32 v51, v81, v50
	v_add_f32_e32 v84, 1.0, v84
	v_add_f32_e32 v85, 1.0, v85
	s_waitcnt lgkmcnt(0)
	v_add_f32_e32 v50, v50, v51
	v_fmamk_f32 v50, v50, 0x3a800000, v234
	v_cmp_gt_f32_e32 vcc, s9, v50
	v_mul_f32_e32 v51, 0x4f800000, v50
	s_nop 0
	v_cndmask_b32_e32 v50, v50, v51, vcc
	v_sqrt_f32_e32 v51, v50
	s_nop 0
	v_add_u32_e32 v90, -1, v51
	v_fma_f32 v91, -v90, v51, v50
	v_cmp_ge_f32_e64 s[36:37], 0, v91
	v_add_u32_e32 v91, 1, v51
	s_nop 0
	v_cndmask_b32_e64 v90, v51, v90, s[36:37]
	v_fma_f32 v51, -v91, v51, v50
	v_cmp_lt_f32_e64 s[36:37], 0, v51
	s_nop 1
	v_cndmask_b32_e64 v51, v90, v91, s[36:37]
	v_mul_f32_e32 v90, 0x37800000, v51
	v_cndmask_b32_e32 v51, v51, v90, vcc
	v_cmp_class_f32_e32 vcc, v50, v232
	s_nop 1
	v_cndmask_b32_e32 v50, v51, v50, vcc
	v_div_scale_f32 v51, s[2:3], v50, v50, 1.0
	v_rcp_f32_e32 v90, v51
	s_nop 0
	v_fma_f32 v91, -v51, v90, 1.0
	v_fmac_f32_e32 v90, v91, v90
	v_div_scale_f32 v91, vcc, 1.0, v50, 1.0
	v_mul_f32_e32 v92, v91, v90
	v_fma_f32 v93, -v51, v92, v91
	v_fmac_f32_e32 v92, v93, v90
	v_fma_f32 v51, -v51, v92, v91
	v_div_fmas_f32 v51, v51, v90, v92
	v_div_fixup_f32 v50, v51, v50, 1.0
	v_pk_mul_f32 v[24:25], v[24:25], v[50:51] op_sel_hi:[1,0]
	s_nop 0
	v_pk_fma_f32 v[90:91], v[106:107], v[24:25], v[110:111]
	v_pk_mul_f32 v[24:25], v[96:97], v[50:51] op_sel_hi:[1,0]
	v_fma_f32 v42, v124, v90, v42
	v_pk_fma_f32 v[92:93], v[108:109], v[24:25], v[112:113]
	v_cvt_pk_bf16_f32 v24, v90, v91
	v_fma_f32 v43, v125, v91, v43
	v_mov_b32_e32 v90, v193
	v_cvt_pk_fp8_f32 v90, v42, v43
	v_pk_mul_f32 v[42:43], v[72:73], v[50:51] op_sel_hi:[1,0]
	v_mov_b32_e32 v91, v193
	v_pk_fma_f32 v[30:31], v[26:27], v[42:43], v[30:31]
	v_pk_mul_f32 v[26:27], v[74:75], v[50:51] op_sel_hi:[1,0]
	v_fma_f32 v12, v86, v30, v12
	v_fma_f32 v13, v87, v31, v13
	v_cvt_pk_fp8_f32 v91, v12, v13
	v_pk_fma_f32 v[28:29], v[28:29], v[26:27], v[32:33]
	v_pk_mul_f32 v[12:13], v[52:53], v[50:51] op_sel_hi:[1,0]
	v_fma_f32 v14, v88, v28, v14
	v_fmac_f32_e32 v15, v89, v29
	v_cvt_pk_fp8_f32 v91, v14, v15 op_sel:[0,0,1]
	v_pk_fma_f32 v[14:15], v[34:35], v[12:13], v[38:39]
	v_pk_mul_f32 v[12:13], v[70:71], v[50:51] op_sel_hi:[1,0]
	v_cvt_pk_bf16_f32 v27, v28, v29
	v_pk_fma_f32 v[28:29], v[36:37], v[12:13], v[40:41]
	v_cvt_pk_bf16_f32 v12, v14, v15
	v_fma_f32 v14, v82, v14, v20
	v_fma_f32 v15, v83, v15, v21
	v_mov_b32_e32 v20, v193
	v_cvt_pk_fp8_f32 v20, v14, v15
	v_pk_mul_f32 v[14:15], v[46:47], v[50:51] op_sel_hi:[1,0]
	v_fma_f32 v21, v84, v28, v22
	v_pk_fma_f32 v[8:9], v[8:9], v[14:15], v[16:17]
	v_fmac_f32_e32 v23, v85, v29
	v_fma_f32 v0, v4, v8, v0
	v_add_f32_e32 v4, 1.0, v5
	v_cvt_pk_fp8_f32 v20, v21, v23 op_sel:[0,0,1]
	v_fma_f32 v1, v4, v9, v1
	v_mov_b32_e32 v21, v193
	v_pk_mul_f32 v[14:15], v[48:49], v[50:51] op_sel_hi:[1,0]
	v_cvt_pk_fp8_f32 v21, v0, v1
	v_pk_fma_f32 v[10:11], v[10:11], v[14:15], v[18:19]
	v_add_f32_e32 v4, 1.0, v6
	v_fma_f32 v44, v126, v92, v44
	v_fmac_f32_e32 v45, v127, v93
	v_fma_f32 v2, v4, v10, v2
	v_add_f32_e32 v4, 1.0, v7
	v_cvt_pk_fp8_f32 v90, v44, v45 op_sel:[0,0,1]
	v_fmac_f32_e32 v3, v4, v11
	v_cvt_pk_fp8_f32 v21, v2, v3 op_sel:[0,0,1]
	v_lshl_add_u64 v[0:1], s[38:39], 0, v[60:61]
	v_add_co_u32_e32 v0, vcc, s0, v0
	v_lshl_add_u64 v[60:61], v[60:61], 0, s[10:11]
	s_nop 0
	v_addc_co_u32_e32 v1, vcc, 0, v1, vcc
	v_cvt_pk_bf16_f32 v25, v92, v93
	v_cvt_pk_bf16_f32 v26, v30, v31
	v_cvt_pk_bf16_f32 v13, v28, v29
	v_cvt_pk_bf16_f32 v14, v8, v9
	v_cvt_pk_bf16_f32 v15, v10, v11
	global_store_dwordx2 v[0:1], v[90:91], off nt
	global_store_dwordx2 v[0:1], v[20:21], off offset:128 nt
	global_store_dwordx4 v[68:69], v[24:27], off nt
	global_store_dwordx4 v[68:69], v[12:15], off offset:256 nt
	s_cbranch_scc1 .LBB0_775
